# input-projection GEMM: six pairs of unit indices exchanged so that no workgroup gets three forget-gate column tiles (heaviest per-workgroup epilogue sum 17.7 -> 15.6 us by instruction count)
# baseline (speedup 1.0000x reference)
.LBB0_217:
	s_add_i32 s73, s73, 1
	s_mul_i32 s9, s73, s27
	v_readlane_b32 s48, v235, 16
	s_add_i32 s9, s9, s48
	v_readlane_b32 s49, v235, 17
	s_cmp_eq_u32 s9, 323
	s_cselect_b32 s99, 198, s9
	s_cmp_eq_u32 s9, 198
	s_cselect_b32 s9, 323, s99
	s_cmp_eq_u32 s9, 331
	s_cselect_b32 s99, 221, s9
	s_cmp_eq_u32 s9, 221
	s_cselect_b32 s9, 331, s99
	s_cmp_eq_u32 s9, 339
	s_cselect_b32 s99, 244, s9
	s_cmp_eq_u32 s9, 244
	s_cselect_b32 s9, 339, s99
	s_cmp_eq_u32 s9, 223
	s_cselect_b32 s99, 284, s9
	s_cmp_eq_u32 s9, 284
	s_cselect_b32 s9, 223, s99
	s_cmp_eq_u32 s9, 231
	s_cselect_b32 s99, 238, s9
	s_cmp_eq_u32 s9, 238
	s_cselect_b32 s9, 231, s99
	s_cmp_eq_u32 s9, 315
	s_cselect_b32 s99, 261, s9
	s_cmp_eq_u32 s9, 261
	s_cselect_b32 s9, 315, s99
	s_cmpk_lt_i32 s9, 0x318
	s_cselect_b64 s[48:49], -1, 0
	s_cmpk_gt_i32 s9, 0x317
	s_cbranch_scc1 .LBB0_219
	s_ashr_i32 s44, s9, 31
	s_lshr_b32 s44, s44, 29
	s_add_i32 s44, s9, s44
	s_ashr_i32 s45, s44, 3
	s_and_b32 s44, s44, -8
	s_sub_i32 s9, s9, s44
	s_cmp_lt_i32 s9, 0
	s_cselect_b32 s44, s76, 0x63
	s_mul_i32 s9, s9, s44
	s_add_i32 s9, s9, s45
	s_mul_hi_i32 s44, s9, 0x2aaaaaab
	s_lshr_b32 s45, s44, 31
	s_ashr_i32 s44, s44, 4
	s_add_i32 s44, s44, s45
	s_lshl_b32 s46, s44, 3
	s_sub_i32 s45, 0x42, s46
	s_min_u32 s47, s45, 8
	s_mulk_i32 s44, 0x60
	s_sub_i32 s9, s9, s44
	v_cvt_f32_ubyte0_e32 v1, s47
	v_cvt_f32_i32_e32 v0, s9
	v_rcp_iflag_f32_e32 v2, v1
	s_ashr_i32 s44, s9, 30
	s_or_b32 s50, s44, 1
	v_mul_f32_e32 v2, v0, v2
	v_trunc_f32_e32 v2, v2
	v_fma_f32 v0, -v2, v1, v0
	v_cvt_i32_f32_e32 v2, v2
	v_cmp_ge_f32_e64 s[44:45], |v0|, v1
	s_and_b64 s[44:45], s[44:45], exec
	s_cselect_b32 s44, s50, 0
	v_readfirstlane_b32 s45, v2
	s_add_i32 s45, s45, s44
	s_sext_i32_i8 s44, s45
	s_mul_i32 s45, s45, s47
	s_sub_i32 s9, s9, s45
	s_sext_i32_i8 s9, s9
	s_add_i32 s46, s46, s9
